# P9 down GEMM: 3 of 8 epilogue store groups moved into MFMA shadow of last K-iteration (on top of peel)
# baseline (speedup 1.0000x reference)
.Lmy_p9_fullepi:
	v_mov_b32_e32 v3, v200
	v_mov_b32_e32 v4, v201
	v_lshlrev_b32_e32 v2, 8, v183
	v_lshlrev_b32_e32 v5, 3, v4
	v_or_b32_e32 v2, s37, v2
	v_and_b32_e32 v5, -16, v5
	v_add_u32_e32 v2, v2, v5
	v_lshlrev_b32_e32 v5, 8, v182
	v_add_u32_e32 v5, s36, v5
	v_lshlrev_b32_e32 v4, 4, v4
	v_add_u32_e32 v10, v5, v3
	v_and_b32_e32 v11, 16, v4
	v_add_u32_e32 v4, v11, v10
	v_ashrrev_i32_e32 v5, 31, v4
	v_lshlrev_b64 v[4:5], 11, v[4:5]
	v_ashrrev_i32_e32 v3, 31, v2
	v_lshl_add_u64 v[4:5], s[14:15], 0, v[4:5]
	v_lshl_add_u64 v[8:9], v[4:5], 0, v[2:3]
	v_med3_f32 v4, v174, s47, v210
	v_med3_f32 v6, v175, s47, v210
	v_med3_f32 v5, v170, s47, v210
	v_med3_f32 v13, v171, s47, v210
	v_cvt_pk_fp8_f32 v4, v4, v6
	v_cvt_pk_fp8_f32 v5, v5, v13
	v_med3_f32 v7, v176, s47, v210
	v_med3_f32 v12, v177, s47, v210
	v_med3_f32 v6, v172, s47, v210
	v_med3_f32 v13, v173, s47, v210
	v_cvt_pk_fp8_f32 v4, v7, v12 op_sel:[0,0,1]
	v_cvt_pk_fp8_f32 v5, v6, v13 op_sel:[0,0,1]
	v_med3_f32 v6, v166, s47, v210
	v_med3_f32 v12, v167, s47, v210
	v_med3_f32 v7, v162, s47, v210
	v_cvt_pk_fp8_f32 v6, v6, v12
	v_med3_f32 v12, v163, s47, v210
	v_cvt_pk_fp8_f32 v7, v7, v12
	v_med3_f32 v13, v168, s47, v210
	v_med3_f32 v14, v169, s47, v210
	v_med3_f32 v12, v164, s47, v210
	v_cvt_pk_fp8_f32 v6, v13, v14 op_sel:[0,0,1]
	v_med3_f32 v13, v165, s47, v210
	v_cvt_pk_fp8_f32 v7, v12, v13 op_sel:[0,0,1]
	v_med3_f32 v13, v155, s47, v210
	v_permlane16_swap_b32_e32 v4, v6
	v_permlane16_swap_b32_e32 v5, v7
	global_store_dwordx4 v[8:9], v[4:7], off
	v_med3_f32 v12, v161, s47, v210
	v_med3_f32 v14, v153, s47, v210
	v_med3_f32 v4, v158, s47, v210
	v_med3_f32 v6, v159, s47, v210
	v_med3_f32 v5, v154, s47, v210
	v_cvt_pk_fp8_f32 v4, v4, v6
	v_cvt_pk_fp8_f32 v5, v5, v13
	v_med3_f32 v7, v160, s47, v210
	v_med3_f32 v6, v156, s47, v210
	v_med3_f32 v13, v157, s47, v210
	v_cvt_pk_fp8_f32 v4, v7, v12 op_sel:[0,0,1]
	v_cvt_pk_fp8_f32 v5, v6, v13 op_sel:[0,0,1]
	v_med3_f32 v6, v150, s47, v210
	v_med3_f32 v12, v151, s47, v210
	v_med3_f32 v7, v146, s47, v210
	v_cvt_pk_fp8_f32 v6, v6, v12
	v_med3_f32 v12, v147, s47, v210
	v_cvt_pk_fp8_f32 v7, v7, v12
	v_med3_f32 v13, v152, s47, v210
	v_med3_f32 v12, v148, s47, v210
	v_cvt_pk_fp8_f32 v6, v13, v14 op_sel:[0,0,1]
	v_med3_f32 v13, v149, s47, v210
	v_cvt_pk_fp8_f32 v7, v12, v13 op_sel:[0,0,1]
	v_or_b32_e32 v12, 32, v11
	v_permlane16_swap_b32_e32 v4, v6
	v_permlane16_swap_b32_e32 v5, v7
	global_store_dwordx4 v[8:9], v[4:7], off offset:128
	v_med3_f32 v14, v139, s47, v210
	v_med3_f32 v13, v145, s47, v210
	v_add_u32_e32 v4, v12, v10
	v_ashrrev_i32_e32 v5, 31, v4
	v_lshlrev_b64 v[4:5], 11, v[4:5]
	v_lshl_add_u64 v[4:5], s[14:15], 0, v[4:5]
	v_lshl_add_u64 v[8:9], v[4:5], 0, v[2:3]
	v_med3_f32 v4, v142, s47, v210
	v_med3_f32 v6, v143, s47, v210
	v_med3_f32 v5, v138, s47, v210
	v_cvt_pk_fp8_f32 v4, v4, v6
	v_cvt_pk_fp8_f32 v5, v5, v14
	v_med3_f32 v7, v144, s47, v210
	v_med3_f32 v6, v140, s47, v210
	v_med3_f32 v14, v141, s47, v210
	v_cvt_pk_fp8_f32 v4, v7, v13 op_sel:[0,0,1]
	v_cvt_pk_fp8_f32 v5, v6, v14 op_sel:[0,0,1]
	v_med3_f32 v6, v134, s47, v210
	v_med3_f32 v13, v135, s47, v210
	v_med3_f32 v7, v122, s47, v210
	v_cvt_pk_fp8_f32 v6, v6, v13
	v_med3_f32 v13, v123, s47, v210
	v_cvt_pk_fp8_f32 v7, v7, v13
	v_med3_f32 v14, v136, s47, v210
	v_med3_f32 v15, v137, s47, v210
	v_med3_f32 v13, v124, s47, v210
	v_cvt_pk_fp8_f32 v6, v14, v15 op_sel:[0,0,1]
	v_med3_f32 v14, v125, s47, v210
	v_cvt_pk_fp8_f32 v7, v13, v14 op_sel:[0,0,1]
	v_med3_f32 v14, v127, s47, v210
	v_permlane16_swap_b32_e32 v4, v6
	v_permlane16_swap_b32_e32 v5, v7
	global_store_dwordx4 v[8:9], v[4:7], off
	v_med3_f32 v13, v133, s47, v210
	v_med3_f32 v15, v121, s47, v210
	v_med3_f32 v4, v130, s47, v210
	v_med3_f32 v6, v131, s47, v210
	v_med3_f32 v5, v126, s47, v210
	v_cvt_pk_fp8_f32 v4, v4, v6
	v_cvt_pk_fp8_f32 v5, v5, v14
	v_med3_f32 v7, v132, s47, v210
	v_med3_f32 v6, v128, s47, v210
	v_med3_f32 v14, v129, s47, v210
	v_cvt_pk_fp8_f32 v4, v7, v13 op_sel:[0,0,1]
	v_cvt_pk_fp8_f32 v5, v6, v14 op_sel:[0,0,1]
	v_med3_f32 v6, v118, s47, v210
	v_med3_f32 v13, v119, s47, v210
	v_med3_f32 v7, v114, s47, v210
	v_cvt_pk_fp8_f32 v6, v6, v13
	v_med3_f32 v13, v115, s47, v210
	v_cvt_pk_fp8_f32 v7, v7, v13
	v_med3_f32 v14, v120, s47, v210
	v_med3_f32 v13, v116, s47, v210
	v_cvt_pk_fp8_f32 v6, v14, v15 op_sel:[0,0,1]
	v_med3_f32 v14, v117, s47, v210
	v_cvt_pk_fp8_f32 v7, v13, v14 op_sel:[0,0,1]
	v_add_u32_e32 v10, 0x80, v10
	v_permlane16_swap_b32_e32 v4, v6
	v_permlane16_swap_b32_e32 v5, v7
	global_store_dwordx4 v[8:9], v[4:7], off offset:128
	v_med3_f32 v13, v107, s47, v210
	v_med3_f32 v14, v105, s47, v210
	v_add_u32_e32 v4, v10, v11
	v_ashrrev_i32_e32 v5, 31, v4
	v_lshlrev_b64 v[4:5], 11, v[4:5]
	v_lshl_add_u64 v[4:5], s[14:15], 0, v[4:5]
	v_lshl_add_u64 v[8:9], v[4:5], 0, v[2:3]
	v_med3_f32 v4, v110, s47, v210
	v_med3_f32 v6, v111, s47, v210
	v_med3_f32 v5, v106, s47, v210
	v_cvt_pk_fp8_f32 v4, v4, v6
	v_cvt_pk_fp8_f32 v5, v5, v13
	v_med3_f32 v7, v112, s47, v210
	v_med3_f32 v11, v113, s47, v210
	v_med3_f32 v6, v108, s47, v210
	v_med3_f32 v13, v109, s47, v210
	v_cvt_pk_fp8_f32 v4, v7, v11 op_sel:[0,0,1]
	v_cvt_pk_fp8_f32 v5, v6, v13 op_sel:[0,0,1]
	v_med3_f32 v6, v102, s47, v210
	v_med3_f32 v11, v103, s47, v210
	v_med3_f32 v7, v98, s47, v210
	v_cvt_pk_fp8_f32 v6, v6, v11
	v_med3_f32 v11, v99, s47, v210
	v_cvt_pk_fp8_f32 v7, v7, v11
	v_med3_f32 v13, v104, s47, v210
	v_med3_f32 v11, v100, s47, v210
	v_cvt_pk_fp8_f32 v6, v13, v14 op_sel:[0,0,1]
	v_med3_f32 v13, v101, s47, v210
	v_cvt_pk_fp8_f32 v7, v11, v13 op_sel:[0,0,1]
	v_med3_f32 v13, v91, s47, v210
	v_permlane16_swap_b32_e32 v4, v6
	v_permlane16_swap_b32_e32 v5, v7
	global_store_dwordx4 v[8:9], v[4:7], off
	v_med3_f32 v11, v97, s47, v210
	v_med3_f32 v14, v89, s47, v210
	v_med3_f32 v4, v94, s47, v210
	v_med3_f32 v6, v95, s47, v210
	v_med3_f32 v5, v90, s47, v210
	v_cvt_pk_fp8_f32 v4, v4, v6
	v_cvt_pk_fp8_f32 v5, v5, v13
	v_med3_f32 v7, v96, s47, v210
	v_med3_f32 v6, v92, s47, v210
	v_med3_f32 v13, v93, s47, v210
	v_cvt_pk_fp8_f32 v4, v7, v11 op_sel:[0,0,1]
	v_cvt_pk_fp8_f32 v5, v6, v13 op_sel:[0,0,1]
	v_med3_f32 v6, v86, s47, v210
	v_med3_f32 v11, v87, s47, v210
	v_med3_f32 v7, v82, s47, v210
	v_cvt_pk_fp8_f32 v6, v6, v11
	v_med3_f32 v11, v83, s47, v210
	v_cvt_pk_fp8_f32 v7, v7, v11
	v_med3_f32 v13, v88, s47, v210
	v_med3_f32 v11, v84, s47, v210
	v_cvt_pk_fp8_f32 v6, v13, v14 op_sel:[0,0,1]
	v_med3_f32 v13, v85, s47, v210
	v_cvt_pk_fp8_f32 v7, v11, v13 op_sel:[0,0,1]
	s_cmp_eq_u32 s40, s30
	v_permlane16_swap_b32_e32 v4, v6
	v_permlane16_swap_b32_e32 v5, v7
	global_store_dwordx4 v[8:9], v[4:7], off offset:128
	v_med3_f32 v9, v75, s47, v210
	v_med3_f32 v8, v81, s47, v210
	v_add_u32_e32 v4, v12, v10
	v_ashrrev_i32_e32 v5, 31, v4
	v_lshlrev_b64 v[4:5], 11, v[4:5]
	v_lshl_add_u64 v[4:5], s[14:15], 0, v[4:5]
	v_lshl_add_u64 v[6:7], v[4:5], 0, v[2:3]
	v_med3_f32 v2, v78, s47, v210
	v_med3_f32 v4, v79, s47, v210
	v_med3_f32 v3, v74, s47, v210
	v_cvt_pk_fp8_f32 v2, v2, v4
	v_cvt_pk_fp8_f32 v3, v3, v9
	v_med3_f32 v5, v80, s47, v210
	v_med3_f32 v4, v76, s47, v210
	v_med3_f32 v9, v77, s47, v210
	v_cvt_pk_fp8_f32 v2, v5, v8 op_sel:[0,0,1]
	v_cvt_pk_fp8_f32 v3, v4, v9 op_sel:[0,0,1]
	v_med3_f32 v4, v70, s47, v210
	v_med3_f32 v8, v71, s47, v210
	v_med3_f32 v5, v66, s47, v210
	v_cvt_pk_fp8_f32 v4, v4, v8
	v_med3_f32 v8, v67, s47, v210
	v_cvt_pk_fp8_f32 v5, v5, v8
	v_med3_f32 v9, v72, s47, v210
	v_med3_f32 v10, v73, s47, v210
	v_med3_f32 v8, v68, s47, v210
	v_cvt_pk_fp8_f32 v4, v9, v10 op_sel:[0,0,1]
	v_med3_f32 v9, v69, s47, v210
	v_cvt_pk_fp8_f32 v5, v8, v9 op_sel:[0,0,1]
	v_med3_f32 v9, v59, s47, v210
	v_permlane16_swap_b32_e32 v2, v4
	v_permlane16_swap_b32_e32 v3, v5
	global_store_dwordx4 v[6:7], v[2:5], off
	v_med3_f32 v8, v65, s47, v210
	v_med3_f32 v10, v57, s47, v210
	v_med3_f32 v2, v62, s47, v210
	v_med3_f32 v4, v63, s47, v210
	v_med3_f32 v3, v58, s47, v210
	v_cvt_pk_fp8_f32 v2, v2, v4
	v_cvt_pk_fp8_f32 v3, v3, v9
	v_med3_f32 v5, v64, s47, v210
	v_med3_f32 v4, v60, s47, v210
	v_med3_f32 v9, v61, s47, v210
	v_cvt_pk_fp8_f32 v2, v5, v8 op_sel:[0,0,1]
	v_cvt_pk_fp8_f32 v3, v4, v9 op_sel:[0,0,1]
	v_med3_f32 v4, v54, s47, v210
	v_med3_f32 v8, v55, s47, v210
	v_med3_f32 v5, v50, s47, v210
	v_cvt_pk_fp8_f32 v4, v4, v8
	v_med3_f32 v8, v51, s47, v210
	v_cvt_pk_fp8_f32 v5, v5, v8
	v_med3_f32 v9, v56, s47, v210
	v_med3_f32 v8, v52, s47, v210
	v_cvt_pk_fp8_f32 v4, v9, v10 op_sel:[0,0,1]
	v_med3_f32 v9, v53, s47, v210
	v_cvt_pk_fp8_f32 v5, v8, v9 op_sel:[0,0,1]
	v_mov_b32_e32 v183, s16
	v_permlane16_swap_b32_e32 v2, v4
	v_permlane16_swap_b32_e32 v3, v5
	v_mov_b32_e32 v182, v178
	s_mov_b64 s[22:23], s[18:19]
	global_store_dwordx4 v[6:7], v[2:5], off offset:128
	s_cbranch_scc1 .LBB0_1677
	s_branch .LBB0_1669
.LBB0_1668:
	v_med3_f32 v130, v130, s47, v210
	v_med3_f32 v131, v131, s47, v210
	v_med3_f32 v132, v132, s47, v210
	v_med3_f32 v133, v133, s47, v210
	v_med3_f32 v126, v126, s47, v210
	v_med3_f32 v127, v127, s47, v210
	v_med3_f32 v128, v128, s47, v210
	v_med3_f32 v129, v129, s47, v210
	v_med3_f32 v118, v118, s47, v210
	v_med3_f32 v119, v119, s47, v210
	v_med3_f32 v120, v120, s47, v210
	v_med3_f32 v121, v121, s47, v210
	v_med3_f32 v114, v114, s47, v210
	v_med3_f32 v115, v115, s47, v210
	v_med3_f32 v116, v116, s47, v210
	v_med3_f32 v117, v117, s47, v210
	v_cvt_pk_fp8_f32 v248, v130, v131
	v_cvt_pk_fp8_f32 v249, v126, v127
	v_cvt_pk_fp8_f32 v250, v118, v119
	v_cvt_pk_fp8_f32 v251, v114, v115
	v_cvt_pk_fp8_f32 v248, v132, v133 op_sel:[0,0,1]
	v_cvt_pk_fp8_f32 v249, v128, v129 op_sel:[0,0,1]
	v_cvt_pk_fp8_f32 v250, v120, v121 op_sel:[0,0,1]
	v_cvt_pk_fp8_f32 v251, v116, v117 op_sel:[0,0,1]
	s_nop 1
	v_permlane16_swap_b32_e32 v248, v250
	v_permlane16_swap_b32_e32 v249, v251
	global_store_dwordx4 v253, v[248:251], s[14:15] offset:128
	v_add_u32_e32 v252, 0x40000, v252
	v_add_u32_e32 v253, 0x40000, v253
	v_med3_f32 v110, v110, s47, v210
	v_med3_f32 v111, v111, s47, v210
	v_med3_f32 v112, v112, s47, v210
	v_med3_f32 v113, v113, s47, v210
	v_med3_f32 v106, v106, s47, v210
	v_med3_f32 v107, v107, s47, v210
	v_med3_f32 v108, v108, s47, v210
	v_med3_f32 v109, v109, s47, v210
	v_med3_f32 v102, v102, s47, v210
	v_med3_f32 v103, v103, s47, v210
	v_med3_f32 v104, v104, s47, v210
	v_med3_f32 v105, v105, s47, v210
	v_med3_f32 v98, v98, s47, v210
	v_med3_f32 v99, v99, s47, v210
	v_med3_f32 v100, v100, s47, v210
	v_med3_f32 v101, v101, s47, v210
	v_cvt_pk_fp8_f32 v248, v110, v111
	v_cvt_pk_fp8_f32 v249, v106, v107
	v_cvt_pk_fp8_f32 v250, v102, v103
	v_cvt_pk_fp8_f32 v251, v98, v99
	v_cvt_pk_fp8_f32 v248, v112, v113 op_sel:[0,0,1]
	v_cvt_pk_fp8_f32 v249, v108, v109 op_sel:[0,0,1]
	v_cvt_pk_fp8_f32 v250, v104, v105 op_sel:[0,0,1]
	v_cvt_pk_fp8_f32 v251, v100, v101 op_sel:[0,0,1]
	s_nop 1
	v_permlane16_swap_b32_e32 v248, v250
	v_permlane16_swap_b32_e32 v249, v251
	global_store_dwordx4 v252, v[248:251], s[14:15]
	v_med3_f32 v94, v94, s47, v210
	v_med3_f32 v95, v95, s47, v210
	v_med3_f32 v96, v96, s47, v210
	v_med3_f32 v97, v97, s47, v210
	v_med3_f32 v90, v90, s47, v210
	v_med3_f32 v91, v91, s47, v210
	v_med3_f32 v92, v92, s47, v210
	v_med3_f32 v93, v93, s47, v210
	v_med3_f32 v86, v86, s47, v210
	v_med3_f32 v87, v87, s47, v210
	v_med3_f32 v88, v88, s47, v210
	v_med3_f32 v89, v89, s47, v210
	v_med3_f32 v82, v82, s47, v210
	v_med3_f32 v83, v83, s47, v210
	v_med3_f32 v84, v84, s47, v210
	v_med3_f32 v85, v85, s47, v210
	v_cvt_pk_fp8_f32 v248, v94, v95
	v_cvt_pk_fp8_f32 v249, v90, v91
	v_cvt_pk_fp8_f32 v250, v86, v87
	v_cvt_pk_fp8_f32 v251, v82, v83
	v_cvt_pk_fp8_f32 v248, v96, v97 op_sel:[0,0,1]
	v_cvt_pk_fp8_f32 v249, v92, v93 op_sel:[0,0,1]
	v_cvt_pk_fp8_f32 v250, v88, v89 op_sel:[0,0,1]
	v_cvt_pk_fp8_f32 v251, v84, v85 op_sel:[0,0,1]
	s_nop 1
	v_permlane16_swap_b32_e32 v248, v250
	v_permlane16_swap_b32_e32 v249, v251
	global_store_dwordx4 v252, v[248:251], s[14:15] offset:128
	v_med3_f32 v78, v78, s47, v210
	v_med3_f32 v79, v79, s47, v210
	v_med3_f32 v80, v80, s47, v210
	v_med3_f32 v81, v81, s47, v210
	v_med3_f32 v74, v74, s47, v210
	v_med3_f32 v75, v75, s47, v210
	v_med3_f32 v76, v76, s47, v210
	v_med3_f32 v77, v77, s47, v210
	v_med3_f32 v70, v70, s47, v210
	v_med3_f32 v71, v71, s47, v210
	v_med3_f32 v72, v72, s47, v210
	v_med3_f32 v73, v73, s47, v210
	v_med3_f32 v66, v66, s47, v210
	v_med3_f32 v67, v67, s47, v210
	v_med3_f32 v68, v68, s47, v210
	v_med3_f32 v69, v69, s47, v210
	v_cvt_pk_fp8_f32 v248, v78, v79
	v_cvt_pk_fp8_f32 v249, v74, v75
	v_cvt_pk_fp8_f32 v250, v70, v71
	v_cvt_pk_fp8_f32 v251, v66, v67
	v_cvt_pk_fp8_f32 v248, v80, v81 op_sel:[0,0,1]
	v_cvt_pk_fp8_f32 v249, v76, v77 op_sel:[0,0,1]
	v_cvt_pk_fp8_f32 v250, v72, v73 op_sel:[0,0,1]
	v_cvt_pk_fp8_f32 v251, v68, v69 op_sel:[0,0,1]
	s_nop 1
	v_permlane16_swap_b32_e32 v248, v250
	v_permlane16_swap_b32_e32 v249, v251
	global_store_dwordx4 v253, v[248:251], s[14:15]
	v_med3_f32 v62, v62, s47, v210
	v_med3_f32 v63, v63, s47, v210
	v_med3_f32 v64, v64, s47, v210
	v_med3_f32 v65, v65, s47, v210
	v_med3_f32 v58, v58, s47, v210
	v_med3_f32 v59, v59, s47, v210
	v_med3_f32 v60, v60, s47, v210
	v_med3_f32 v61, v61, s47, v210
	v_med3_f32 v54, v54, s47, v210
	v_med3_f32 v55, v55, s47, v210
	v_med3_f32 v56, v56, s47, v210
	v_med3_f32 v57, v57, s47, v210
	v_med3_f32 v50, v50, s47, v210
	v_med3_f32 v51, v51, s47, v210
	v_med3_f32 v52, v52, s47, v210
	v_med3_f32 v53, v53, s47, v210
	v_cvt_pk_fp8_f32 v248, v62, v63
	v_cvt_pk_fp8_f32 v249, v58, v59
	v_cvt_pk_fp8_f32 v250, v54, v55
	v_cvt_pk_fp8_f32 v251, v50, v51
	v_cvt_pk_fp8_f32 v248, v64, v65 op_sel:[0,0,1]
	v_cvt_pk_fp8_f32 v249, v60, v61 op_sel:[0,0,1]
	v_cvt_pk_fp8_f32 v250, v56, v57 op_sel:[0,0,1]
	v_cvt_pk_fp8_f32 v251, v52, v53 op_sel:[0,0,1]
	s_nop 1
	v_permlane16_swap_b32_e32 v248, v250
	v_permlane16_swap_b32_e32 v249, v251
	global_store_dwordx4 v253, v[248:251], s[14:15] offset:128
	s_cmp_eq_u32 s40, s30
	v_mov_b32_e32 v183, s16
	v_mov_b32_e32 v182, v178
	s_mov_b64 s[22:23], s[18:19]
	s_cbranch_scc1 .LBB0_1677

.LBB0_1675:
	s_add_i32 s59, s59, 2
	s_add_u32 s24, s22, 0x100
	s_addc_u32 s25, s23, 0
	s_and_b64 s[28:29], s[26:27], exec
	s_cselect_b32 s28, 0, s24
	s_cselect_b32 s29, 0, s25
	s_add_u32 s28, s12, s28
	s_addc_u32 s29, s13, s29
	s_add_u32 s60, s57, s22
	s_addc_u32 s61, s58, s23
	s_and_b64 s[22:23], s[26:27], exec
	s_cselect_b32 s23, s55, s61
	s_cselect_b32 s22, s56, s60
	s_mov_b32 m0, s5
	s_waitcnt lgkmcnt(0)
	v_mfma_scale_f32_16x16x128_f8f6f4 v[222:225], v[2:9], v[42:49], v[142:145], v209, v208 op_sel_hi:[0,0,0]
	v_lshl_add_u64 v[238:239], s[22:23], 0, v[188:189]
	v_add_u32_e32 v191, s46, v203
	v_lshl_add_u64 v[240:241], s[22:23], 0, v[186:187]
	v_mov_b32_e32 v193, v185
	v_mov_b32_e32 v195, v185
	s_nop 1
	v_add_u32_e32 v142, s46, v202
	v_mfma_scale_f32_16x16x128_f8f6f4 v[226:229], v[10:17], v[42:49], v[138:141], v209, v208 op_sel_hi:[0,0,0]
	s_nop 6
	ds_read_b128 v[138:141], v142
	ds_read_b128 v[214:217], v142 offset:2048
	ds_read_b128 v[142:145], v191
	ds_read_b128 v[218:221], v191 offset:2048
	global_load_lds_dwordx4 v[238:239], off
	s_mov_b32 m0, s31
	s_nop 0
	global_load_lds_dwordx4 v[240:241], off
	v_mfma_scale_f32_16x16x128_f8f6f4 v[174:177], v[2:9], v[26:33], v[174:177], v209, v208 op_sel_hi:[0,0,0]
	s_barrier
	s_waitcnt lgkmcnt(0)
	v_mfma_scale_f32_16x16x128_f8f6f4 v[170:173], v[10:17], v[26:33], v[170:173], v209, v208 op_sel_hi:[0,0,0]
	v_mfma_scale_f32_16x16x128_f8f6f4 v[166:169], v[2:9], v[18:25], v[166:169], v209, v208 op_sel_hi:[0,0,0]
	v_mfma_scale_f32_16x16x128_f8f6f4 v[162:165], v[10:17], v[18:25], v[162:165], v209, v208 op_sel_hi:[0,0,0]
	v_mfma_scale_f32_16x16x128_f8f6f4 v[134:137], v[2:9], v[34:41], v[134:137], v209, v208 op_sel_hi:[0,0,0]
	v_mfma_scale_f32_16x16x128_f8f6f4 v[122:125], v[10:17], v[34:41], v[122:125], v209, v208 op_sel_hi:[0,0,0]
	s_setprio 1
	s_waitcnt lgkmcnt(0)
	v_mfma_scale_f32_16x16x128_f8f6f4 v[158:161], v[138:145], v[26:33], v[158:161], v209, v208 op_sel_hi:[0,0,0]
	v_mfma_scale_f32_16x16x128_f8f6f4 v[154:157], v[214:221], v[26:33], v[154:157], v209, v208 op_sel_hi:[0,0,0]
	v_mfma_scale_f32_16x16x128_f8f6f4 v[150:153], v[138:145], v[18:25], v[150:153], v209, v208 op_sel_hi:[0,0,0]
	v_mfma_scale_f32_16x16x128_f8f6f4 v[146:149], v[214:221], v[18:25], v[146:149], v209, v208 op_sel_hi:[0,0,0]
	v_mfma_scale_f32_16x16x128_f8f6f4 v[130:133], v[138:145], v[42:49], v[130:133], v209, v208 op_sel_hi:[0,0,0]
	v_mfma_scale_f32_16x16x128_f8f6f4 v[126:129], v[214:221], v[42:49], v[126:129], v209, v208 op_sel_hi:[0,0,0]
	v_mfma_scale_f32_16x16x128_f8f6f4 v[118:121], v[138:145], v[34:41], v[118:121], v209, v208 op_sel_hi:[0,0,0]
	v_mfma_scale_f32_16x16x128_f8f6f4 v[114:117], v[214:221], v[34:41], v[114:117], v209, v208 op_sel_hi:[0,0,0]
	s_setprio 0
	s_mov_b32 m0, s4
	s_barrier
	ds_read_b128 v[18:21], v206 offset:16384
	ds_read_b128 v[26:29], v206 offset:18432
	ds_read_b128 v[22:25], v207 offset:16384
	ds_read_b128 v[30:33], v207 offset:18432
	ds_read_b128 v[34:37], v206 offset:20480
	ds_read_b128 v[42:45], v206 offset:22528
	ds_read_b128 v[38:41], v207 offset:20480
	ds_read_b128 v[46:49], v207 offset:22528
	global_load_lds_dwordx4 v184, s[28:29]
	s_mov_b32 m0, s33
	v_mov_b32_e32 v191, v185
	global_load_lds_dwordx4 v190, s[28:29]
	s_barrier
	s_waitcnt lgkmcnt(0)
	v_lshl_add_u64 v[242:243], s[28:29], 0, v[184:185]
	v_lshl_add_u64 v[244:245], s[28:29], 0, v[190:191]
	s_setprio 1
	s_waitcnt lgkmcnt(0)
	v_mfma_scale_f32_16x16x128_f8f6f4 v[110:113], v[2:9], v[18:25], v[110:113], v209, v208 op_sel_hi:[0,0,0]
	v_mfma_scale_f32_16x16x128_f8f6f4 v[106:109], v[10:17], v[18:25], v[106:109], v209, v208 op_sel_hi:[0,0,0]
	v_mfma_scale_f32_16x16x128_f8f6f4 v[102:105], v[2:9], v[26:33], v[102:105], v209, v208 op_sel_hi:[0,0,0]
	v_mfma_scale_f32_16x16x128_f8f6f4 v[98:101], v[10:17], v[26:33], v[98:101], v209, v208 op_sel_hi:[0,0,0]
	v_mfma_scale_f32_16x16x128_f8f6f4 v[78:81], v[2:9], v[34:41], v[78:81], v209, v208 op_sel_hi:[0,0,0]
	v_mfma_scale_f32_16x16x128_f8f6f4 v[74:77], v[10:17], v[34:41], v[74:77], v209, v208 op_sel_hi:[0,0,0]
	v_mfma_scale_f32_16x16x128_f8f6f4 v[70:73], v[2:9], v[42:49], v[70:73], v209, v208 op_sel_hi:[0,0,0]
	v_mfma_scale_f32_16x16x128_f8f6f4 v[66:69], v[10:17], v[42:49], v[66:69], v209, v208 op_sel_hi:[0,0,0]
	s_setprio 0
	s_barrier
	s_add_u32 s26, s22, 0x10000
	s_addc_u32 s27, s23, 0
	s_mov_b32 m0, s48
	v_lshl_add_u64 v[2:3], s[26:27], 0, v[188:189]
	global_load_lds_dwordx4 v[2:3], off
	v_lshl_add_u64 v[2:3], s[26:27], 0, v[186:187]
	s_mov_b32 m0, s49
	s_nop 0
	global_load_lds_dwordx4 v[2:3], off
	s_waitcnt vmcnt(6)
	s_barrier
	s_setprio 1
	v_mfma_scale_f32_16x16x128_f8f6f4 v[94:97], v[138:145], v[18:25], v[94:97], v209, v208 op_sel_hi:[0,0,0]
	v_mfma_scale_f32_16x16x128_f8f6f4 v[90:93], v[214:221], v[18:25], v[90:93], v209, v208 op_sel_hi:[0,0,0]
	v_mfma_scale_f32_16x16x128_f8f6f4 v[86:89], v[138:145], v[26:33], v[86:89], v209, v208 op_sel_hi:[0,0,0]
	v_mfma_scale_f32_16x16x128_f8f6f4 v[82:85], v[214:221], v[26:33], v[82:85], v209, v208 op_sel_hi:[0,0,0]
	v_mfma_scale_f32_16x16x128_f8f6f4 v[62:65], v[138:145], v[34:41], v[62:65], v209, v208 op_sel_hi:[0,0,0]
	v_mfma_scale_f32_16x16x128_f8f6f4 v[58:61], v[214:221], v[34:41], v[58:61], v209, v208 op_sel_hi:[0,0,0]
	v_mfma_scale_f32_16x16x128_f8f6f4 v[230:233], v[138:145], v[42:49], v[54:57], v209, v208 op_sel_hi:[0,0,0]
	v_mfma_scale_f32_16x16x128_f8f6f4 v[234:237], v[214:221], v[42:49], v[50:53], v209, v208 op_sel_hi:[0,0,0]
	s_setprio 0
	v_add_u32_e32 v6, s50, v202
	v_add_u32_e32 v14, s50, v203
	s_barrier
	ds_read_b128 v[2:5], v6
	ds_read_b128 v[10:13], v6 offset:2048
	ds_read_b128 v[6:9], v14
	ds_read_b128 v[14:17], v14 offset:2048
	s_mov_b32 m0, s34
	v_lshl_add_u64 v[50:51], s[28:29], 0, v[192:193]
	ds_read_b128 v[18:21], v206 offset:32768
	ds_read_b128 v[26:29], v206 offset:34816
	ds_read_b128 v[22:25], v207 offset:32768
	ds_read_b128 v[30:33], v207 offset:34816
	ds_read_b128 v[34:37], v206 offset:36864
	ds_read_b128 v[42:45], v206 offset:38912
	ds_read_b128 v[38:41], v207 offset:36864
	ds_read_b128 v[46:49], v207 offset:38912
	global_load_lds_dwordx4 v[50:51], off
	v_lshl_add_u64 v[50:51], s[28:29], 0, v[194:195]
	s_mov_b32 m0, s35
	s_nop 0
	global_load_lds_dwordx4 v[50:51], off
	s_waitcnt lgkmcnt(8)
	s_barrier
	s_waitcnt lgkmcnt(0)
	s_setprio 1
	s_waitcnt lgkmcnt(0)
	v_mfma_scale_f32_16x16x128_f8f6f4 v[174:177], v[2:9], v[18:25], v[174:177], v209, v208 op_sel_hi:[0,0,0]
	v_lshl_or_b32 v246, v183, 8, s37
	v_lshlrev_b32_e32 v247, 3, v201
	v_mfma_scale_f32_16x16x128_f8f6f4 v[170:173], v[10:17], v[18:25], v[170:173], v209, v208 op_sel_hi:[0,0,0]
	v_and_b32_e32 v247, -16, v247
	v_add_u32_e32 v246, v246, v247
	v_mfma_scale_f32_16x16x128_f8f6f4 v[166:169], v[2:9], v[26:33], v[166:169], v209, v208 op_sel_hi:[0,0,0]
	v_lshl_add_u32 v247, v182, 8, v200
	v_mfma_scale_f32_16x16x128_f8f6f4 v[162:165], v[10:17], v[26:33], v[162:165], v209, v208 op_sel_hi:[0,0,0]
	v_add_u32_e32 v247, s36, v247
	v_mfma_scale_f32_16x16x128_f8f6f4 v[142:145], v[2:9], v[34:41], v[222:225], v209, v208 op_sel_hi:[0,0,0]
	v_lshlrev_b32_e32 v254, 4, v201
	v_mfma_scale_f32_16x16x128_f8f6f4 v[138:141], v[10:17], v[34:41], v[226:229], v209, v208 op_sel_hi:[0,0,0]
	v_and_b32_e32 v254, 16, v254
	v_mfma_scale_f32_16x16x128_f8f6f4 v[134:137], v[2:9], v[42:49], v[134:137], v209, v208 op_sel_hi:[0,0,0]
	v_add_u32_e32 v247, v247, v254
	v_mfma_scale_f32_16x16x128_f8f6f4 v[122:125], v[10:17], v[42:49], v[122:125], v209, v208 op_sel_hi:[0,0,0]
	v_lshl_add_u32 v252, v247, 11, v246
	v_add_u32_e32 v253, 0x10000, v252
	s_setprio 0
	s_barrier
	s_mov_b32 m0, s52
	v_add_u32_e32 v54, s51, v202
	v_lshl_add_u64 v[222:223], v[238:239], 0, s[8:9]
	v_add_u32_e32 v191, s51, v203
	ds_read_b128 v[50:53], v54
	ds_read_b128 v[214:217], v54 offset:2048
	ds_read_b128 v[54:57], v191
	ds_read_b128 v[218:221], v191 offset:2048
	global_load_lds_dwordx4 v[222:223], off
	v_lshl_add_u64 v[222:223], v[240:241], 0, s[8:9]
	s_mov_b32 m0, s53
	s_nop 0
	global_load_lds_dwordx4 v[222:223], off
	s_barrier
	s_waitcnt lgkmcnt(0)
	s_setprio 1
	s_waitcnt lgkmcnt(0)
	v_mfma_scale_f32_16x16x128_f8f6f4 v[158:161], v[50:57], v[18:25], v[158:161], v209, v208 op_sel_hi:[0,0,0]
	v_med3_f32 v174, v174, s47, v210
	v_med3_f32 v175, v175, s47, v210
	v_med3_f32 v176, v176, s47, v210
	v_med3_f32 v177, v177, s47, v210
	v_mfma_scale_f32_16x16x128_f8f6f4 v[154:157], v[214:221], v[18:25], v[154:157], v209, v208 op_sel_hi:[0,0,0]
	v_med3_f32 v170, v170, s47, v210
	v_med3_f32 v171, v171, s47, v210
	v_med3_f32 v172, v172, s47, v210
	v_med3_f32 v173, v173, s47, v210
	v_mfma_scale_f32_16x16x128_f8f6f4 v[150:153], v[50:57], v[26:33], v[150:153], v209, v208 op_sel_hi:[0,0,0]
	v_med3_f32 v166, v166, s47, v210
	v_med3_f32 v167, v167, s47, v210
	v_med3_f32 v168, v168, s47, v210
	v_med3_f32 v169, v169, s47, v210
	v_mfma_scale_f32_16x16x128_f8f6f4 v[146:149], v[214:221], v[26:33], v[146:149], v209, v208 op_sel_hi:[0,0,0]
	v_med3_f32 v162, v162, s47, v210
	v_med3_f32 v163, v163, s47, v210
	v_med3_f32 v164, v164, s47, v210
	v_med3_f32 v165, v165, s47, v210
	v_mfma_scale_f32_16x16x128_f8f6f4 v[130:133], v[50:57], v[34:41], v[130:133], v209, v208 op_sel_hi:[0,0,0]
	v_cvt_pk_fp8_f32 v248, v174, v175
	v_cvt_pk_fp8_f32 v249, v170, v171
	v_cvt_pk_fp8_f32 v250, v166, v167
	v_cvt_pk_fp8_f32 v251, v162, v163
	v_mfma_scale_f32_16x16x128_f8f6f4 v[126:129], v[214:221], v[34:41], v[126:129], v209, v208 op_sel_hi:[0,0,0]
	v_cvt_pk_fp8_f32 v248, v176, v177 op_sel:[0,0,1]
	v_cvt_pk_fp8_f32 v249, v172, v173 op_sel:[0,0,1]
	v_mfma_scale_f32_16x16x128_f8f6f4 v[118:121], v[50:57], v[42:49], v[118:121], v209, v208 op_sel_hi:[0,0,0]
	v_cvt_pk_fp8_f32 v250, v168, v169 op_sel:[0,0,1]
	v_cvt_pk_fp8_f32 v251, v164, v165 op_sel:[0,0,1]
	v_mfma_scale_f32_16x16x128_f8f6f4 v[114:117], v[214:221], v[42:49], v[114:117], v209, v208 op_sel_hi:[0,0,0]
	s_nop 0
	v_permlane16_swap_b32_e32 v248, v250
	v_permlane16_swap_b32_e32 v249, v251
	global_store_dwordx4 v252, v[248:251], s[14:15]
	s_setprio 0
	s_mov_b32 m0, s38
	v_lshl_add_u64 v[222:223], v[242:243], 0, s[8:9]
	s_barrier
	ds_read_b128 v[18:21], v206 offset:49152
	ds_read_b128 v[26:29], v206 offset:51200
	ds_read_b128 v[22:25], v207 offset:49152
	ds_read_b128 v[30:33], v207 offset:51200
	ds_read_b128 v[34:37], v206 offset:53248
	ds_read_b128 v[42:45], v206 offset:55296
	ds_read_b128 v[38:41], v207 offset:53248
	ds_read_b128 v[46:49], v207 offset:55296
	global_load_lds_dwordx4 v[222:223], off
	v_lshl_add_u64 v[222:223], v[244:245], 0, s[8:9]
	s_mov_b32 m0, s39
	s_nop 0
	global_load_lds_dwordx4 v[222:223], off
	s_barrier
	s_waitcnt lgkmcnt(0)
	s_setprio 1
	s_waitcnt lgkmcnt(0)
	v_mfma_scale_f32_16x16x128_f8f6f4 v[110:113], v[2:9], v[18:25], v[110:113], v209, v208 op_sel_hi:[0,0,0]
	v_med3_f32 v142, v142, s47, v210
	v_med3_f32 v143, v143, s47, v210
	v_med3_f32 v144, v144, s47, v210
	v_med3_f32 v145, v145, s47, v210
	v_mfma_scale_f32_16x16x128_f8f6f4 v[106:109], v[10:17], v[18:25], v[106:109], v209, v208 op_sel_hi:[0,0,0]
	v_med3_f32 v138, v138, s47, v210
	v_med3_f32 v139, v139, s47, v210
	v_med3_f32 v140, v140, s47, v210
	v_med3_f32 v141, v141, s47, v210
	v_mfma_scale_f32_16x16x128_f8f6f4 v[102:105], v[2:9], v[26:33], v[102:105], v209, v208 op_sel_hi:[0,0,0]
	v_med3_f32 v134, v134, s47, v210
	v_med3_f32 v135, v135, s47, v210
	v_med3_f32 v136, v136, s47, v210
	v_med3_f32 v137, v137, s47, v210
	v_mfma_scale_f32_16x16x128_f8f6f4 v[98:101], v[10:17], v[26:33], v[98:101], v209, v208 op_sel_hi:[0,0,0]
	v_med3_f32 v122, v122, s47, v210
	v_med3_f32 v123, v123, s47, v210
	v_med3_f32 v124, v124, s47, v210
	v_med3_f32 v125, v125, s47, v210
	v_mfma_scale_f32_16x16x128_f8f6f4 v[78:81], v[2:9], v[34:41], v[78:81], v209, v208 op_sel_hi:[0,0,0]
	v_cvt_pk_fp8_f32 v248, v142, v143
	v_cvt_pk_fp8_f32 v249, v138, v139
	v_cvt_pk_fp8_f32 v250, v134, v135
	v_cvt_pk_fp8_f32 v251, v122, v123
	v_mfma_scale_f32_16x16x128_f8f6f4 v[74:77], v[10:17], v[34:41], v[74:77], v209, v208 op_sel_hi:[0,0,0]
	v_cvt_pk_fp8_f32 v248, v144, v145 op_sel:[0,0,1]
	v_cvt_pk_fp8_f32 v249, v140, v141 op_sel:[0,0,1]
	v_mfma_scale_f32_16x16x128_f8f6f4 v[70:73], v[2:9], v[42:49], v[70:73], v209, v208 op_sel_hi:[0,0,0]
	v_cvt_pk_fp8_f32 v250, v136, v137 op_sel:[0,0,1]
	v_cvt_pk_fp8_f32 v251, v124, v125 op_sel:[0,0,1]
	v_mfma_scale_f32_16x16x128_f8f6f4 v[66:69], v[10:17], v[42:49], v[66:69], v209, v208 op_sel_hi:[0,0,0]
	s_nop 0
	v_permlane16_swap_b32_e32 v248, v250
	v_permlane16_swap_b32_e32 v249, v251
	global_store_dwordx4 v253, v[248:251], s[14:15]
	s_setprio 0
	s_barrier
	s_add_u32 s22, s22, 0x10080
	s_addc_u32 s23, s23, 0
	s_mov_b32 m0, s54
	v_lshl_add_u64 v[2:3], s[22:23], 0, v[188:189]
	global_load_lds_dwordx4 v[2:3], off
	v_lshl_add_u64 v[2:3], s[22:23], 0, v[186:187]
	s_add_i32 m0, s54, 0x2000
	s_nop 0
	global_load_lds_dwordx4 v[2:3], off
	s_waitcnt vmcnt(8)
	s_barrier
	s_setprio 1
	v_mfma_scale_f32_16x16x128_f8f6f4 v[94:97], v[50:57], v[18:25], v[94:97], v209, v208 op_sel_hi:[0,0,0]
	v_med3_f32 v158, v158, s47, v210
	v_med3_f32 v159, v159, s47, v210
	v_med3_f32 v160, v160, s47, v210
	v_med3_f32 v161, v161, s47, v210
	v_mfma_scale_f32_16x16x128_f8f6f4 v[90:93], v[214:221], v[18:25], v[90:93], v209, v208 op_sel_hi:[0,0,0]
	v_med3_f32 v154, v154, s47, v210
	v_med3_f32 v155, v155, s47, v210
	v_med3_f32 v156, v156, s47, v210
	v_med3_f32 v157, v157, s47, v210
	v_mfma_scale_f32_16x16x128_f8f6f4 v[86:89], v[50:57], v[26:33], v[86:89], v209, v208 op_sel_hi:[0,0,0]
	v_med3_f32 v150, v150, s47, v210
	v_med3_f32 v151, v151, s47, v210
	v_med3_f32 v152, v152, s47, v210
	v_med3_f32 v153, v153, s47, v210
	v_mfma_scale_f32_16x16x128_f8f6f4 v[82:85], v[214:221], v[26:33], v[82:85], v209, v208 op_sel_hi:[0,0,0]
	v_med3_f32 v146, v146, s47, v210
	v_med3_f32 v147, v147, s47, v210
	v_med3_f32 v148, v148, s47, v210
	v_med3_f32 v149, v149, s47, v210
	v_mfma_scale_f32_16x16x128_f8f6f4 v[62:65], v[50:57], v[34:41], v[62:65], v209, v208 op_sel_hi:[0,0,0]
	v_cvt_pk_fp8_f32 v248, v158, v159
	v_cvt_pk_fp8_f32 v249, v154, v155
	v_cvt_pk_fp8_f32 v250, v150, v151
	v_cvt_pk_fp8_f32 v251, v146, v147
	v_mfma_scale_f32_16x16x128_f8f6f4 v[58:61], v[214:221], v[34:41], v[58:61], v209, v208 op_sel_hi:[0,0,0]
	v_cvt_pk_fp8_f32 v248, v160, v161 op_sel:[0,0,1]
	v_cvt_pk_fp8_f32 v249, v156, v157 op_sel:[0,0,1]
	v_mfma_scale_f32_16x16x128_f8f6f4 v[54:57], v[50:57], v[42:49], v[230:233], v209, v208 op_sel_hi:[0,0,0]
	v_cvt_pk_fp8_f32 v250, v152, v153 op_sel:[0,0,1]
	v_cvt_pk_fp8_f32 v251, v148, v149 op_sel:[0,0,1]
	v_mfma_scale_f32_16x16x128_f8f6f4 v[50:53], v[214:221], v[42:49], v[234:237], v209, v208 op_sel_hi:[0,0,0]
	s_nop 0
	v_permlane16_swap_b32_e32 v248, v250
	v_permlane16_swap_b32_e32 v249, v251
	global_store_dwordx4 v252, v[248:251], s[14:15] offset:128
	s_setprio 0
	s_cmp_ge_i32 s59, s1
	s_barrier
	s_cbranch_scc1 .LBB0_1668
	s_mov_b64 s[22:23], s[24:25]
	s_branch .LBB0_1673
